# phase-start code prefetch: 64 KiB window, each workgroup touches its 8 KiB slice ((wg>>3)&7)
# baseline (speedup 1.0000x reference)
_Z4mega5MArgs:
	v_lshlrev_b32_e32 v250, 6, v0
	s_lshr_b32 s100, s2, 3
	s_and_b32 s100, s100, 7
	s_lshl_b32 s100, s100, 13
	v_lshlrev_b32_e32 v251, 4, v0
	v_add_u32_e32 v251, s100, v251
	v_accvgpr_write_b32 a1, v251
	s_load_dwordx4 s[28:31], s[0:1], 0xe0
	s_load_dword s33, s[0:1], 0xf0
	s_add_u32 s4, s0, 0xf0
	s_addc_u32 s5, s1, 0
	v_lshrrev_b32_e32 v1, 6, v0
	s_nop 1
	v_readfirstlane_b32 s98, v1
	v_and_b32_e32 v1, 63, v0
	v_writelane_b32 v249, s4, 0
	v_cmp_eq_u32_e32 vcc, 0, v1
	s_nop 0
	v_writelane_b32 v249, s5, 1
	s_and_saveexec_b64 s[4:5], vcc
	s_cbranch_execz .LBB0_2
	s_getreg_b32 s3, hwreg(HW_REG_HW_ID, 0, 6)
	s_lshl_b32 s3, s3, 2
	s_and_b32 s3, s3, 0xfc
	s_add_i32 s3, s3, 0
	s_add_i32 s3, s3, 0x25c00
	v_lshrrev_b32_e32 v1, 6, v0
	v_mov_b32_e32 v2, s3
	ds_write_b32 v2, v1

.LBB0_2122:
	s_or_b64 exec, exec, s[0:1]
	s_barrier
	v_accvgpr_read_b32 v251, a1
	s_getpc_b64 s[100:101]
	v_min_u32_e32 v251, 0xf980, v251
	global_load_dword a0, v251, s[100:101]

.LBB0_2301:
	s_or_b64 exec, exec, s[0:1]
	s_barrier
	v_accvgpr_read_b32 v251, a1
	s_getpc_b64 s[100:101]
	v_min_u32_e32 v251, 0xab80, v251
	global_load_dword a0, v251, s[100:101]
